# speedup vs baseline: 1.0292x; 1.0292x over previous
.Lk1_nowarm0:
	s_and_b32 s15, s2, 7
	s_lshl_b32 s15, s15, 2
	s_lshr_b32 s17, s2, 6
	s_add_u32 s15, s15, s17
	s_bfe_u32 s16, s2, 0x30003
	s_mul_i32 s17, s16, 0x271
	v_add_u32_e32 v2, s17, v0
	v_lshlrev_b32_e32 v1, 2, v2
	s_movk_i32 s17, 0x271
	v_cmp_gt_u32_e32 vcc, s17, v0
	s_and_b64 exec, exec, vcc
	s_mov_b64 s[18:19], exec
	s_lshr_b32 s21, s21, 6
	s_movk_i32 s13, 0x4e20
	s_mov_b32 s14, 0x3fb8aa3b
	s_mov_b32 s12, 0
	s_mov_b32 s10, 0x13d620
	s_mov_b32 s11, 0x20000
	s_mul_i32 s17, s15, 0x13d620
	s_mul_hi_u32 s20, s15, 0x13d620
	s_mov_b32 s40, 0
	s_add_u32 s41, s40, s13
	s_add_u32 s42, s41, s13
	s_add_u32 s43, s42, s13
	s_add_u32 s44, s43, s13
	s_add_u32 s45, s44, s13
	s_add_u32 s46, s45, s13
	s_add_u32 s47, s46, s13
	s_add_u32 s48, s47, s13
	s_add_u32 s49, s48, s13
	s_add_u32 s50, s49, s13
	s_add_u32 s51, s50, s13
	s_add_u32 s52, s51, s13
	s_add_u32 s53, s52, s13
	s_add_u32 s54, s53, s13
	s_add_u32 s55, s54, s13
	s_waitcnt lgkmcnt(0)
	s_add_u32 s8, s4, s17
	s_addc_u32 s9, s5, s20
	s_and_b32 s9, s9, 0xffff
	buffer_load_dword v8, v1, s[8:11], s40 offen nt
	buffer_load_dword v9, v1, s[8:11], s41 offen nt
	buffer_load_dword v10, v1, s[8:11], s42 offen nt
	buffer_load_dword v11, v1, s[8:11], s43 offen nt
	buffer_load_dword v12, v1, s[8:11], s44 offen nt
	buffer_load_dword v13, v1, s[8:11], s45 offen nt
	buffer_load_dword v14, v1, s[8:11], s46 offen nt
	buffer_load_dword v15, v1, s[8:11], s47 offen nt
	buffer_load_dword v16, v1, s[8:11], s48 offen nt
	buffer_load_dword v17, v1, s[8:11], s49 offen nt
	buffer_load_dword v18, v1, s[8:11], s50 offen nt
	buffer_load_dword v19, v1, s[8:11], s51 offen nt
	buffer_load_dword v20, v1, s[8:11], s52 offen nt
	buffer_load_dword v21, v1, s[8:11], s53 offen nt
	buffer_load_dword v22, v1, s[8:11], s54 offen nt
	buffer_load_dword v23, v1, s[8:11], s55 offen nt
	s_add_u32 s8, s8, 0x4e200
	s_addc_u32 s9, s9, 0
	buffer_load_dword v24, v1, s[8:11], s40 offen nt
	buffer_load_dword v25, v1, s[8:11], s41 offen nt
	buffer_load_dword v26, v1, s[8:11], s42 offen nt
	buffer_load_dword v27, v1, s[8:11], s43 offen nt
	buffer_load_dword v28, v1, s[8:11], s44 offen nt
	buffer_load_dword v29, v1, s[8:11], s45 offen nt
	buffer_load_dword v30, v1, s[8:11], s46 offen nt
	buffer_load_dword v31, v1, s[8:11], s47 offen nt
	buffer_load_dword v32, v1, s[8:11], s48 offen nt
	buffer_load_dword v33, v1, s[8:11], s49 offen nt
	buffer_load_dword v34, v1, s[8:11], s50 offen nt
	buffer_load_dword v35, v1, s[8:11], s51 offen nt
	buffer_load_dword v36, v1, s[8:11], s52 offen nt
	buffer_load_dword v37, v1, s[8:11], s53 offen nt
	buffer_load_dword v38, v1, s[8:11], s54 offen nt
	buffer_load_dword v39, v1, s[8:11], s55 offen nt
	s_add_u32 s8, s8, 0x4e200
	s_addc_u32 s9, s9, 0
	buffer_load_dword v40, v1, s[8:11], s40 offen nt
	buffer_load_dword v41, v1, s[8:11], s41 offen nt
	buffer_load_dword v42, v1, s[8:11], s42 offen nt
	buffer_load_dword v43, v1, s[8:11], s43 offen nt
	buffer_load_dword v44, v1, s[8:11], s44 offen nt
	buffer_load_dword v45, v1, s[8:11], s45 offen nt
	buffer_load_dword v46, v1, s[8:11], s46 offen nt
	buffer_load_dword v47, v1, s[8:11], s47 offen nt
	buffer_load_dword v48, v1, s[8:11], s48 offen nt
	buffer_load_dword v49, v1, s[8:11], s49 offen nt
	buffer_load_dword v50, v1, s[8:11], s50 offen nt
	buffer_load_dword v51, v1, s[8:11], s51 offen nt
	buffer_load_dword v52, v1, s[8:11], s52 offen nt
	buffer_load_dword v53, v1, s[8:11], s53 offen nt
	buffer_load_dword v54, v1, s[8:11], s54 offen nt
	buffer_load_dword v55, v1, s[8:11], s55 offen nt
	s_add_u32 s8, s8, 0x4e200
	s_addc_u32 s9, s9, 0
	buffer_load_dword v56, v1, s[8:11], s40 offen nt
	buffer_load_dword v57, v1, s[8:11], s41 offen nt
	buffer_load_dword v58, v1, s[8:11], s42 offen nt
	buffer_load_dword v59, v1, s[8:11], s43 offen nt
	buffer_load_dword v60, v1, s[8:11], s44 offen nt
	buffer_load_dword v61, v1, s[8:11], s45 offen nt
	buffer_load_dword v62, v1, s[8:11], s46 offen nt
	buffer_load_dword v63, v1, s[8:11], s47 offen nt
	buffer_load_dword v64, v1, s[8:11], s48 offen nt
	buffer_load_dword v65, v1, s[8:11], s49 offen nt
	buffer_load_dword v66, v1, s[8:11], s50 offen nt
	v_mul_u32_u24_e32 v3, 0x147b, v2
	v_lshrrev_b32_e32 v3, 19, v3
	v_mul_u32_u24_e32 v98, 0x64, v3
	v_sub_u32_e32 v98, v2, v98
	v_add_u32_e32 v3, -1, v3
	v_add_u32_e32 v98, -1, v98
	s_movk_i32 s17, 0x62
	v_cmp_gt_u32_e64 s[36:37], 48, v3
	v_cmp_gt_u32_e64 s[38:39], s17, v98
	s_mul_i32 s17, s15, 0x1388
	v_add_lshl_u32 v98, v2, s17, 3
	s_and_b64 s[36:37], s[36:37], s[38:39]
	s_waitcnt vmcnt(55)
	buffer_load_dword v67, v1, s[8:11], s51 offen nt
	buffer_load_dword v68, v1, s[8:11], s52 offen nt
	buffer_load_dword v69, v1, s[8:11], s53 offen nt
	buffer_load_dword v70, v1, s[8:11], s54 offen nt
	buffer_load_dword v71, v1, s[8:11], s55 offen nt
	s_add_u32 s8, s8, 0x4e200
	s_addc_u32 s9, s9, 0
	buffer_load_dword v72, v1, s[8:11], s40 offen nt
	s_cmp_eq_u32 s21, 9
	s_cselect_b32 s17, 1, 0
	s_cmp_eq_u32 s16, 0
	s_cselect_b32 s17, s17, 0
	s_cmp_lg_u32 s17, 0
	s_cbranch_scc0 .Lk1_nowarm9
	s_mul_i32 s22, s15, 0x3a9800
	v_writelane_b32 v3, s22, 0
	s_add_u32 s23, s22, 0x10000
	v_writelane_b32 v3, s23, 1
	s_add_u32 s22, s22, 0x138800
	v_writelane_b32 v3, s22, 2
	s_add_u32 s23, s22, 0x10000
	v_writelane_b32 v3, s23, 3
	s_add_u32 s22, s22, 0x138800
	v_writelane_b32 v3, s22, 4
	s_add_u32 s23, s22, 0x10000
	v_writelane_b32 v3, s23, 5
	s_mov_b64 exec, 63
	global_load_dword v92, v3, s[32:33]
	s_mul_i32 s22, s15, 0x12c00
	s_add_u32 s22, s22, 0x1c200
	v_writelane_b32 v3, s22, 0
	s_add_u32 s22, s22, 0x10000
	v_writelane_b32 v3, s22, 1
	s_mul_i32 s22, s15, 0xe10
	v_writelane_b32 v3, s22, 2
	s_mul_i32 s22, s15, 0x4b0
	s_add_u32 s22, s22, 0x274200
	v_writelane_b32 v3, s22, 3
	s_mov_b64 exec, 15
	global_load_dword v93, v3, s[34:35]
	s_mov_b64 exec, s[18:19]
.Lk1_nowarm9:
	s_waitcnt vmcnt(49)
	v_max3_f32 v76, v8, v9, v10
	v_max3_f32 v76, v76, v11, v12
	v_max3_f32 v76, v76, v13, v14
	v_max3_f32 v76, v76, v15, v16
	v_max3_f32 v76, v76, v17, v18
	v_max3_f32 v76, v76, v19, v20
	v_max3_f32 v76, v76, v21, v22
	v_max_f32_e32 v76, v76, v23
	v_pk_add_f32 v[8:9], v[8:9], v[76:77] op_sel_hi:[1,0] neg_lo:[0,1] neg_hi:[0,1]
	v_pk_add_f32 v[10:11], v[10:11], v[76:77] op_sel_hi:[1,0] neg_lo:[0,1] neg_hi:[0,1]
	v_pk_add_f32 v[12:13], v[12:13], v[76:77] op_sel_hi:[1,0] neg_lo:[0,1] neg_hi:[0,1]
	v_pk_add_f32 v[14:15], v[14:15], v[76:77] op_sel_hi:[1,0] neg_lo:[0,1] neg_hi:[0,1]
	v_pk_add_f32 v[16:17], v[16:17], v[76:77] op_sel_hi:[1,0] neg_lo:[0,1] neg_hi:[0,1]
	v_pk_add_f32 v[18:19], v[18:19], v[76:77] op_sel_hi:[1,0] neg_lo:[0,1] neg_hi:[0,1]
	v_pk_add_f32 v[20:21], v[20:21], v[76:77] op_sel_hi:[1,0] neg_lo:[0,1] neg_hi:[0,1]
	v_pk_add_f32 v[22:23], v[22:23], v[76:77] op_sel_hi:[1,0] neg_lo:[0,1] neg_hi:[0,1]
	v_or_b32_e32 v81, 0, v8
	v_or_b32_e32 v82, 1, v9
	v_min_u32_e32 v80, v81, v82
	v_or_b32_e32 v81, 2, v10
	v_or_b32_e32 v82, 3, v11
	v_min3_u32 v80, v80, v81, v82
	v_or_b32_e32 v81, 4, v12
	v_or_b32_e32 v82, 5, v13
	v_min3_u32 v80, v80, v81, v82
	v_or_b32_e32 v81, 6, v14
	v_or_b32_e32 v82, 7, v15
	v_min3_u32 v80, v80, v81, v82
	v_or_b32_e32 v81, 8, v16
	v_or_b32_e32 v82, 9, v17
	v_min3_u32 v80, v80, v81, v82
	v_or_b32_e32 v81, 10, v18
	v_or_b32_e32 v82, 11, v19
	v_min3_u32 v80, v80, v81, v82
	v_or_b32_e32 v81, 12, v20
	v_or_b32_e32 v82, 13, v21
	v_min3_u32 v80, v80, v81, v82
	v_or_b32_e32 v81, 14, v22
	v_or_b32_e32 v82, 15, v23
	v_min3_u32 v80, v80, v81, v82
	v_pk_mul_f32 v[8:9], v[8:9], s[14:15] op_sel_hi:[1,0]
	v_pk_mul_f32 v[10:11], v[10:11], s[14:15] op_sel_hi:[1,0]
	v_pk_mul_f32 v[12:13], v[12:13], s[14:15] op_sel_hi:[1,0]
	v_pk_mul_f32 v[14:15], v[14:15], s[14:15] op_sel_hi:[1,0]
	v_pk_mul_f32 v[16:17], v[16:17], s[14:15] op_sel_hi:[1,0]
	v_pk_mul_f32 v[18:19], v[18:19], s[14:15] op_sel_hi:[1,0]
	v_pk_mul_f32 v[20:21], v[20:21], s[14:15] op_sel_hi:[1,0]
	v_pk_mul_f32 v[22:23], v[22:23], s[14:15] op_sel_hi:[1,0]
	v_exp_f32_e32 v8, v8
	v_exp_f32_e32 v9, v9
	v_exp_f32_e32 v10, v10
	v_exp_f32_e32 v11, v11
	v_exp_f32_e32 v12, v12
	v_exp_f32_e32 v13, v13
	v_exp_f32_e32 v14, v14
	v_exp_f32_e32 v15, v15
	v_exp_f32_e32 v16, v16
	v_exp_f32_e32 v17, v17
	v_exp_f32_e32 v18, v18
	v_exp_f32_e32 v19, v19
	v_exp_f32_e32 v20, v20
	v_exp_f32_e32 v21, v21
	v_exp_f32_e32 v22, v22
	v_exp_f32_e32 v23, v23
	v_pk_add_f32 v[78:79], v[8:9], v[10:11]
	v_pk_add_f32 v[78:79], v[78:79], v[12:13]
	v_pk_add_f32 v[78:79], v[78:79], v[14:15]
	v_pk_add_f32 v[78:79], v[78:79], v[16:17]
	v_pk_add_f32 v[78:79], v[78:79], v[18:19]
	v_pk_add_f32 v[78:79], v[78:79], v[20:21]
	v_pk_add_f32 v[78:79], v[78:79], v[22:23]
	v_add_f32_e32 v78, v78, v79
	v_cvt_f64_f32_e32 v[86:87], v78
	v_mov_b32_e32 v75, v80
	v_mov_b32_e32 v73, v76
	s_waitcnt vmcnt(33)
	v_max3_f32 v76, v24, v25, v26
	v_max3_f32 v76, v76, v27, v28
	v_max3_f32 v76, v76, v29, v30
	v_max3_f32 v76, v76, v31, v32
	v_max3_f32 v76, v76, v33, v34
	v_max3_f32 v76, v76, v35, v36
	v_max3_f32 v76, v76, v37, v38
	v_max_f32_e32 v76, v76, v39
	v_max_f32_e32 v100, v73, v76
	v_cmp_gt_f32_e64 s[26:27], v76, v73
	v_sub_f32_e32 v83, v73, v100
	v_mul_f32_e32 v83, s14, v83
	v_exp_f32_e32 v83, v83
	v_pk_add_f32 v[24:25], v[24:25], v[100:101] op_sel_hi:[1,0] neg_lo:[0,1] neg_hi:[0,1]
	v_pk_add_f32 v[26:27], v[26:27], v[100:101] op_sel_hi:[1,0] neg_lo:[0,1] neg_hi:[0,1]
	v_pk_add_f32 v[28:29], v[28:29], v[100:101] op_sel_hi:[1,0] neg_lo:[0,1] neg_hi:[0,1]
	v_pk_add_f32 v[30:31], v[30:31], v[100:101] op_sel_hi:[1,0] neg_lo:[0,1] neg_hi:[0,1]
	v_pk_add_f32 v[32:33], v[32:33], v[100:101] op_sel_hi:[1,0] neg_lo:[0,1] neg_hi:[0,1]
	v_pk_add_f32 v[34:35], v[34:35], v[100:101] op_sel_hi:[1,0] neg_lo:[0,1] neg_hi:[0,1]
	v_pk_add_f32 v[36:37], v[36:37], v[100:101] op_sel_hi:[1,0] neg_lo:[0,1] neg_hi:[0,1]
	v_pk_add_f32 v[38:39], v[38:39], v[100:101] op_sel_hi:[1,0] neg_lo:[0,1] neg_hi:[0,1]
	v_cvt_f64_f32_e32 v[90:91], v83
	v_or_b32_e32 v81, 16, v24
	v_or_b32_e32 v82, 17, v25
	v_min_u32_e32 v80, v81, v82
	v_or_b32_e32 v81, 18, v26
	v_or_b32_e32 v82, 19, v27
	v_min3_u32 v80, v80, v81, v82
	v_or_b32_e32 v81, 20, v28
	v_or_b32_e32 v82, 21, v29
	v_min3_u32 v80, v80, v81, v82
	v_or_b32_e32 v81, 22, v30
	v_or_b32_e32 v82, 23, v31
	v_min3_u32 v80, v80, v81, v82
	v_or_b32_e32 v81, 24, v32
	v_or_b32_e32 v82, 25, v33
	v_min3_u32 v80, v80, v81, v82
	v_or_b32_e32 v81, 26, v34
	v_or_b32_e32 v82, 27, v35
	v_min3_u32 v80, v80, v81, v82
	v_or_b32_e32 v81, 28, v36
	v_or_b32_e32 v82, 29, v37
	v_min3_u32 v80, v80, v81, v82
	v_or_b32_e32 v81, 30, v38
	v_or_b32_e32 v82, 31, v39
	v_min3_u32 v80, v80, v81, v82
	v_pk_mul_f32 v[24:25], v[24:25], s[14:15] op_sel_hi:[1,0]
	v_pk_mul_f32 v[26:27], v[26:27], s[14:15] op_sel_hi:[1,0]
	v_pk_mul_f32 v[28:29], v[28:29], s[14:15] op_sel_hi:[1,0]
	v_pk_mul_f32 v[30:31], v[30:31], s[14:15] op_sel_hi:[1,0]
	v_pk_mul_f32 v[32:33], v[32:33], s[14:15] op_sel_hi:[1,0]
	v_pk_mul_f32 v[34:35], v[34:35], s[14:15] op_sel_hi:[1,0]
	v_pk_mul_f32 v[36:37], v[36:37], s[14:15] op_sel_hi:[1,0]
	v_pk_mul_f32 v[38:39], v[38:39], s[14:15] op_sel_hi:[1,0]
	v_exp_f32_e32 v24, v24
	v_exp_f32_e32 v25, v25
	v_exp_f32_e32 v26, v26
	v_exp_f32_e32 v27, v27
	v_exp_f32_e32 v28, v28
	v_exp_f32_e32 v29, v29
	v_exp_f32_e32 v30, v30
	v_exp_f32_e32 v31, v31
	v_exp_f32_e32 v32, v32
	v_exp_f32_e32 v33, v33
	v_exp_f32_e32 v34, v34
	v_exp_f32_e32 v35, v35
	v_exp_f32_e32 v36, v36
	v_exp_f32_e32 v37, v37
	v_exp_f32_e32 v38, v38
	v_exp_f32_e32 v39, v39
	v_pk_add_f32 v[78:79], v[24:25], v[26:27]
	v_pk_add_f32 v[78:79], v[78:79], v[28:29]
	v_pk_add_f32 v[78:79], v[78:79], v[30:31]
	v_pk_add_f32 v[78:79], v[78:79], v[32:33]
	v_pk_add_f32 v[78:79], v[78:79], v[34:35]
	v_pk_add_f32 v[78:79], v[78:79], v[36:37]
	v_pk_add_f32 v[78:79], v[78:79], v[38:39]
	v_add_f32_e32 v78, v78, v79
	v_cvt_f64_f32_e32 v[84:85], v78
	v_cndmask_b32_e64 v75, v75, v80, s[26:27]
	v_mov_b32_e32 v73, v100
	v_fma_f64 v[86:87], v[86:87], v[90:91], v[84:85]
	s_waitcnt vmcnt(17)
	v_max3_f32 v76, v40, v41, v42
	v_max3_f32 v76, v76, v43, v44
	v_max3_f32 v76, v76, v45, v46
	v_max3_f32 v76, v76, v47, v48
	v_max3_f32 v76, v76, v49, v50
	v_max3_f32 v76, v76, v51, v52
	v_max3_f32 v76, v76, v53, v54
	v_max_f32_e32 v76, v76, v55
	v_max_f32_e32 v100, v73, v76
	v_cmp_gt_f32_e64 s[26:27], v76, v73
	v_sub_f32_e32 v83, v73, v100
	v_mul_f32_e32 v83, s14, v83
	v_exp_f32_e32 v83, v83
	v_pk_add_f32 v[40:41], v[40:41], v[100:101] op_sel_hi:[1,0] neg_lo:[0,1] neg_hi:[0,1]
	v_pk_add_f32 v[42:43], v[42:43], v[100:101] op_sel_hi:[1,0] neg_lo:[0,1] neg_hi:[0,1]
	v_pk_add_f32 v[44:45], v[44:45], v[100:101] op_sel_hi:[1,0] neg_lo:[0,1] neg_hi:[0,1]
	v_pk_add_f32 v[46:47], v[46:47], v[100:101] op_sel_hi:[1,0] neg_lo:[0,1] neg_hi:[0,1]
	v_pk_add_f32 v[48:49], v[48:49], v[100:101] op_sel_hi:[1,0] neg_lo:[0,1] neg_hi:[0,1]
	v_pk_add_f32 v[50:51], v[50:51], v[100:101] op_sel_hi:[1,0] neg_lo:[0,1] neg_hi:[0,1]
	v_pk_add_f32 v[52:53], v[52:53], v[100:101] op_sel_hi:[1,0] neg_lo:[0,1] neg_hi:[0,1]
	v_pk_add_f32 v[54:55], v[54:55], v[100:101] op_sel_hi:[1,0] neg_lo:[0,1] neg_hi:[0,1]
	v_cvt_f64_f32_e32 v[90:91], v83
	v_or_b32_e32 v81, 32, v40
	v_or_b32_e32 v82, 33, v41
	v_min_u32_e32 v80, v81, v82
	v_or_b32_e32 v81, 34, v42
	v_or_b32_e32 v82, 35, v43
	v_min3_u32 v80, v80, v81, v82
	v_or_b32_e32 v81, 36, v44
	v_or_b32_e32 v82, 37, v45
	v_min3_u32 v80, v80, v81, v82
	v_or_b32_e32 v81, 38, v46
	v_or_b32_e32 v82, 39, v47
	v_min3_u32 v80, v80, v81, v82
	v_or_b32_e32 v81, 40, v48
	v_or_b32_e32 v82, 41, v49
	v_min3_u32 v80, v80, v81, v82
	v_or_b32_e32 v81, 42, v50
	v_or_b32_e32 v82, 43, v51
	v_min3_u32 v80, v80, v81, v82
	v_or_b32_e32 v81, 44, v52
	v_or_b32_e32 v82, 45, v53
	v_min3_u32 v80, v80, v81, v82
	v_or_b32_e32 v81, 46, v54
	v_or_b32_e32 v82, 47, v55
	v_min3_u32 v80, v80, v81, v82
	v_pk_mul_f32 v[40:41], v[40:41], s[14:15] op_sel_hi:[1,0]
	v_pk_mul_f32 v[42:43], v[42:43], s[14:15] op_sel_hi:[1,0]
	v_pk_mul_f32 v[44:45], v[44:45], s[14:15] op_sel_hi:[1,0]
	v_pk_mul_f32 v[46:47], v[46:47], s[14:15] op_sel_hi:[1,0]
	v_pk_mul_f32 v[48:49], v[48:49], s[14:15] op_sel_hi:[1,0]
	v_pk_mul_f32 v[50:51], v[50:51], s[14:15] op_sel_hi:[1,0]
	v_pk_mul_f32 v[52:53], v[52:53], s[14:15] op_sel_hi:[1,0]
	v_pk_mul_f32 v[54:55], v[54:55], s[14:15] op_sel_hi:[1,0]
	v_exp_f32_e32 v40, v40
	v_exp_f32_e32 v41, v41
	v_exp_f32_e32 v42, v42
	v_exp_f32_e32 v43, v43
	v_exp_f32_e32 v44, v44
	v_exp_f32_e32 v45, v45
	v_exp_f32_e32 v46, v46
	v_exp_f32_e32 v47, v47
	v_exp_f32_e32 v48, v48
	v_exp_f32_e32 v49, v49
	v_exp_f32_e32 v50, v50
	v_exp_f32_e32 v51, v51
	v_exp_f32_e32 v52, v52
	v_exp_f32_e32 v53, v53
	v_exp_f32_e32 v54, v54
	v_exp_f32_e32 v55, v55
	v_pk_add_f32 v[78:79], v[40:41], v[42:43]
	v_pk_add_f32 v[78:79], v[78:79], v[44:45]
	v_pk_add_f32 v[78:79], v[78:79], v[46:47]
	v_pk_add_f32 v[78:79], v[78:79], v[48:49]
	v_pk_add_f32 v[78:79], v[78:79], v[50:51]
	v_pk_add_f32 v[78:79], v[78:79], v[52:53]
	v_pk_add_f32 v[78:79], v[78:79], v[54:55]
	v_add_f32_e32 v78, v78, v79
	v_cvt_f64_f32_e32 v[84:85], v78
	v_cndmask_b32_e64 v75, v75, v80, s[26:27]
	v_mov_b32_e32 v73, v100
	v_fma_f64 v[86:87], v[86:87], v[90:91], v[84:85]
	s_waitcnt vmcnt(9)
	v_max3_f32 v76, v56, v57, v58
	v_max3_f32 v76, v76, v59, v60
	v_max3_f32 v76, v76, v61, v62
	v_max_f32_e32 v76, v76, v63
	v_max_f32_e32 v100, v73, v76
	v_cmp_gt_f32_e64 s[26:27], v76, v73
	v_sub_f32_e32 v83, v73, v100
	v_mul_f32_e32 v83, s14, v83
	v_exp_f32_e32 v83, v83
	v_pk_add_f32 v[56:57], v[56:57], v[100:101] op_sel_hi:[1,0] neg_lo:[0,1] neg_hi:[0,1]
	v_pk_add_f32 v[58:59], v[58:59], v[100:101] op_sel_hi:[1,0] neg_lo:[0,1] neg_hi:[0,1]
	v_pk_add_f32 v[60:61], v[60:61], v[100:101] op_sel_hi:[1,0] neg_lo:[0,1] neg_hi:[0,1]
	v_pk_add_f32 v[62:63], v[62:63], v[100:101] op_sel_hi:[1,0] neg_lo:[0,1] neg_hi:[0,1]
	v_cvt_f64_f32_e32 v[90:91], v83
	v_or_b32_e32 v81, 48, v56
	v_or_b32_e32 v82, 49, v57
	v_min_u32_e32 v80, v81, v82
	v_or_b32_e32 v81, 50, v58
	v_or_b32_e32 v82, 51, v59
	v_min3_u32 v80, v80, v81, v82
	v_or_b32_e32 v81, 52, v60
	v_or_b32_e32 v82, 53, v61
	v_min3_u32 v80, v80, v81, v82
	v_or_b32_e32 v81, 54, v62
	v_or_b32_e32 v82, 55, v63
	v_min3_u32 v80, v80, v81, v82
	v_pk_mul_f32 v[56:57], v[56:57], s[14:15] op_sel_hi:[1,0]
	v_pk_mul_f32 v[58:59], v[58:59], s[14:15] op_sel_hi:[1,0]
	v_pk_mul_f32 v[60:61], v[60:61], s[14:15] op_sel_hi:[1,0]
	v_pk_mul_f32 v[62:63], v[62:63], s[14:15] op_sel_hi:[1,0]
	v_exp_f32_e32 v56, v56
	v_exp_f32_e32 v57, v57
	v_exp_f32_e32 v58, v58
	v_exp_f32_e32 v59, v59
	v_exp_f32_e32 v60, v60
	v_exp_f32_e32 v61, v61
	v_exp_f32_e32 v62, v62
	v_exp_f32_e32 v63, v63
	v_pk_add_f32 v[78:79], v[56:57], v[58:59]
	v_pk_add_f32 v[78:79], v[78:79], v[60:61]
	v_pk_add_f32 v[78:79], v[78:79], v[62:63]
	v_add_f32_e32 v78, v78, v79
	v_cvt_f64_f32_e32 v[84:85], v78
	v_cndmask_b32_e64 v75, v75, v80, s[26:27]
	v_mov_b32_e32 v73, v100
	v_fma_f64 v[86:87], v[86:87], v[90:91], v[84:85]
	s_waitcnt vmcnt(5)
	v_max3_f32 v76, v64, v65, v66
	v_max_f32_e32 v76, v76, v67
	v_max_f32_e32 v100, v73, v76
	v_cmp_gt_f32_e64 s[26:27], v76, v73
	v_sub_f32_e32 v83, v73, v100
	v_mul_f32_e32 v83, s14, v83
	v_exp_f32_e32 v83, v83
	v_pk_add_f32 v[64:65], v[64:65], v[100:101] op_sel_hi:[1,0] neg_lo:[0,1] neg_hi:[0,1]
	v_pk_add_f32 v[66:67], v[66:67], v[100:101] op_sel_hi:[1,0] neg_lo:[0,1] neg_hi:[0,1]
	v_cvt_f64_f32_e32 v[90:91], v83
	v_or_b32_e32 v81, 56, v64
	v_or_b32_e32 v82, 57, v65
	v_min_u32_e32 v80, v81, v82
	v_or_b32_e32 v81, 58, v66
	v_or_b32_e32 v82, 59, v67
	v_min3_u32 v80, v80, v81, v82
	v_pk_mul_f32 v[64:65], v[64:65], s[14:15] op_sel_hi:[1,0]
	v_pk_mul_f32 v[66:67], v[66:67], s[14:15] op_sel_hi:[1,0]
	v_exp_f32_e32 v64, v64
	v_exp_f32_e32 v65, v65
	v_exp_f32_e32 v66, v66
	v_exp_f32_e32 v67, v67
	s_nop 0
	v_pk_add_f32 v[78:79], v[64:65], v[66:67]
	v_add_f32_e32 v78, v78, v79
	v_cvt_f64_f32_e32 v[84:85], v78
	v_cndmask_b32_e64 v75, v75, v80, s[26:27]
	v_mov_b32_e32 v73, v100
	v_fma_f64 v[86:87], v[86:87], v[90:91], v[84:85]
	s_waitcnt vmcnt(0)
	v_max3_f32 v76, v68, v69, v70
	v_max3_f32 v76, v76, v71, v72
	v_max_f32_e32 v100, v73, v76
	v_cmp_gt_f32_e64 s[26:27], v76, v73
	v_sub_f32_e32 v83, v73, v100
	v_mul_f32_e32 v83, s14, v83
	v_exp_f32_e32 v83, v83
	v_pk_add_f32 v[68:69], v[68:69], v[100:101] op_sel_hi:[1,0] neg_lo:[0,1] neg_hi:[0,1]
	v_pk_add_f32 v[70:71], v[70:71], v[100:101] op_sel_hi:[1,0] neg_lo:[0,1] neg_hi:[0,1]
	v_sub_f32_e32 v72, v72, v100
	v_cvt_f64_f32_e32 v[90:91], v83
	v_or_b32_e32 v81, 60, v68
	v_or_b32_e32 v82, 61, v69
	v_min_u32_e32 v80, v81, v82
	v_or_b32_e32 v81, 62, v70
	v_or_b32_e32 v82, 63, v71
	v_min3_u32 v80, v80, v81, v82
	v_or_b32_e32 v81, 64, v72
	v_min_u32_e32 v80, v80, v81
	v_pk_mul_f32 v[68:69], v[68:69], s[14:15] op_sel_hi:[1,0]
	v_pk_mul_f32 v[70:71], v[70:71], s[14:15] op_sel_hi:[1,0]
	v_mul_f32_e32 v72, s14, v72
	v_exp_f32_e32 v68, v68
	v_exp_f32_e32 v69, v69
	v_exp_f32_e32 v70, v70
	v_exp_f32_e32 v71, v71
	v_exp_f32_e32 v72, v72
	v_cndmask_b32_e64 v75, v75, v80, s[26:27]
	v_pk_add_f32 v[78:79], v[68:69], v[70:71]
	v_add_f32_e32 v78, v78, v79
	v_add_f32_e32 v78, v78, v72
	v_cvt_f64_f32_e32 v[84:85], v78
	v_fma_f64 v[86:87], v[86:87], v[90:91], v[84:85]
	v_rcp_f64_e32 v[88:89], v[86:87]
	v_cmp_gt_u32_e32 vcc, 64, v75
	s_and_b64 vcc, vcc, s[36:37]
	v_fma_f64 v[90:91], -v[86:87], v[88:89], 1.0
	v_fma_f64 v[88:89], v[90:91], v[88:89], v[88:89]
	v_cvt_f32_f64_e32 v3, v[88:89]
	v_cndmask_b32_e32 v74, 0, v3, vcc
	global_store_dwordx2 v98, v[74:75], s[6:7]
